# v43 + k_readout prologue de-serialised: first mask-list entry requested together with mcnt
# speedup vs baseline: 1.0148x; 1.0148x over previous
_Z9k_readoutPKDv4_jPKfPKiPK15HIP_vector_typeIiLj2EES3_S3_S3_PfSA_:
	s_load_dwordx4 s[4:7], s[0:1], 0x0
	s_load_dwordx2 s[8:9], s[0:1], 0x10
	s_load_dwordx2 s[12:13], s[0:1], 0x18
	v_lshrrev_b32_e32 v53, 6, v0
	v_lshl_or_b32 v44, s2, 2, v53
	v_ashrrev_i32_e32 v45, 31, v44
	v_and_b32_e32 v52, 63, v0
	s_waitcnt lgkmcnt(0)
	v_lshl_add_u64 v[2:3], v[44:45], 2, s[8:9]
	global_load_dword v57, v[2:3], off
	v_mov_b32_e32 v9, 0
	v_lshlrev_b64 v[2:3], 8, v[44:45]
	v_lshl_add_u64 v[2:3], s[6:7], 0, v[2:3]
	v_lshlrev_b32_e32 v46, 2, v52
	v_mov_b32_e32 v47, v9
	v_lshl_add_u64 v[2:3], v[2:3], 0, v[46:47]
	v_add_co_u32_e32 v4, vcc, 0x200000, v2
	s_load_dwordx2 s[6:7], s[0:1], 0x30
	s_nop 0
	v_addc_co_u32_e32 v5, vcc, 0, v3, vcc
	global_load_dword v48, v[2:3], off
	global_load_dword v49, v[4:5], off
	v_lshlrev_b64 v[10:11], 10, v[44:45]
	v_lshl_add_u64 v[10:11], s[12:13], 0, v[10:11]
	v_lshlrev_b32_e32 v12, 3, v52
	v_mov_b32_e32 v13, 0
	v_lshl_add_u64 v[10:11], v[10:11], 0, v[12:13]
	global_load_dwordx2 v[24:25], v[10:11], off
	v_bfe_u32 v54, v0, 5, 1
	s_waitcnt lgkmcnt(0)
	s_load_dword s2, s[6:7], 0x0
	s_movk_i32 s6, 0x80
	v_and_b32_e32 v47, 7, v0
	v_lshlrev_b32_e32 v8, 20, v54
	s_mov_b32 s3, 0
	v_bfe_u32 v55, v0, 3, 2
	v_mbcnt_lo_u32_b32 v56, -1, 0
	s_waitcnt vmcnt(3)
	v_cmp_lt_i32_e32 vcc, s6, v57
	s_and_saveexec_b64 s[6:7], vcc
	s_xor_b64 s[6:7], exec, s[6:7]
	s_cbranch_execz .LBB4_10
	s_load_dwordx2 s[8:9], s[0:1], 0x20
	v_lshl_add_u64 v[0:1], s[4:5], 0, v[8:9]
	v_lshlrev_b32_e32 v8, 4, v47
	v_lshlrev_b64 v[2:3], 15, v[44:45]
	v_lshl_add_u64 v[16:17], v[0:1], 0, v[8:9]
	v_mbcnt_hi_u32_b32 v1, -1, v56
	s_waitcnt lgkmcnt(0)
	v_lshl_add_u64 v[18:19], s[8:9], 0, v[2:3]
	v_lshlrev_b32_e32 v0, 2, v55
	v_mov_b32_e32 v8, v9
	v_lshlrev_b32_e32 v1, 2, v1
	s_movk_i32 s8, 0x100
	v_mov_b32_e32 v10, v9
	v_mov_b32_e32 v11, v9
	v_mov_b32_e32 v12, v9
	v_mov_b32_e32 v13, v9
	v_mov_b32_e32 v14, v9
	v_mov_b32_e32 v15, v9
	v_and_or_b32 v23, v1, s8, v0
	v_mov_b64_e32 v[0:1], v[8:9]
	v_mov_b32_e32 v22, 0
	v_mov_b64_e32 v[2:3], v[10:11]
	v_mov_b64_e32 v[4:5], v[12:13]
	v_mov_b64_e32 v[6:7], v[14:15]

.LBB4_9:
.LBB4_10:
	s_andn2_saveexec_b64 s[6:7], s[6:7]
	s_cbranch_execz .LBB4_18
	s_load_dwordx2 s[8:9], s[0:1], 0x18
	v_lshlrev_b64 v[0:1], 10, v[44:45]
	v_lshlrev_b32_e32 v50, 3, v52
	v_mov_b32_e32 v51, 0
	v_or_b32_e32 v2, 64, v52
	s_waitcnt lgkmcnt(0)
	v_lshl_add_u64 v[0:1], s[8:9], 0, v[0:1]
	v_lshl_add_u64 v[0:1], v[0:1], 0, v[50:51]
	v_cmp_lt_i32_e32 vcc, v2, v57
	v_mov_b32_e32 v50, v44
	s_and_saveexec_b64 s[8:9], vcc
	s_cbranch_execz .LBB4_13
	global_load_dwordx2 v[50:51], v[0:1], off offset:512

	.amdhsa_kernel _Z9k_readoutPKDv4_jPKfPKiPK15HIP_vector_typeIiLj2EES3_S3_S3_PfSA_
		.amdhsa_group_segment_fixed_size 6144
		.amdhsa_private_segment_fixed_size 0
		.amdhsa_kernarg_size 72
		.amdhsa_user_sgpr_count 2
		.amdhsa_user_sgpr_dispatch_ptr 0
		.amdhsa_user_sgpr_queue_ptr 0
		.amdhsa_user_sgpr_kernarg_segment_ptr 1
		.amdhsa_user_sgpr_dispatch_id 0
		.amdhsa_user_sgpr_kernarg_preload_length 0
		.amdhsa_user_sgpr_kernarg_preload_offset 0
		.amdhsa_user_sgpr_private_segment_size 0
		.amdhsa_uses_dynamic_stack 0
		.amdhsa_enable_private_segment 0
		.amdhsa_system_sgpr_workgroup_id_x 1
		.amdhsa_system_sgpr_workgroup_id_y 0
		.amdhsa_system_sgpr_workgroup_id_z 0
		.amdhsa_system_sgpr_workgroup_info 0
		.amdhsa_system_vgpr_workitem_id 0
		.amdhsa_next_free_vgpr 92
		.amdhsa_next_free_sgpr 14
		.amdhsa_accum_offset 92
		.amdhsa_reserve_vcc 1
		.amdhsa_float_round_mode_32 0
		.amdhsa_float_round_mode_16_64 0
		.amdhsa_float_denorm_mode_32 3
		.amdhsa_float_denorm_mode_16_64 3
		.amdhsa_dx10_clamp 1
		.amdhsa_ieee_mode 1
		.amdhsa_fp16_overflow 0
		.amdhsa_tg_split 0
		.amdhsa_exception_fp_ieee_invalid_op 0
		.amdhsa_exception_fp_denorm_src 0
		.amdhsa_exception_fp_ieee_div_zero 0
		.amdhsa_exception_fp_ieee_overflow 0
		.amdhsa_exception_fp_ieee_underflow 0
		.amdhsa_exception_fp_ieee_inexact 0
		.amdhsa_exception_int_div_zero 0
	.end_amdhsa_kernel

amdhsa.kernels:
  - .agpr_count:     0
    .args:
      - .actual_access:  read_only
        .address_space:  global
        .offset:         0
        .size:           8
        .value_kind:     global_buffer
      - .actual_access:  read_only
        .address_space:  global
        .offset:         8
        .size:           8
        .value_kind:     global_buffer
      - .actual_access:  read_only
        .address_space:  global
        .offset:         16
        .size:           8
        .value_kind:     global_buffer
      - .actual_access:  write_only
        .address_space:  global
        .offset:         24
        .size:           8
        .value_kind:     global_buffer
      - .actual_access:  write_only
        .address_space:  global
        .offset:         32
        .size:           8
        .value_kind:     global_buffer
      - .actual_access:  write_only
        .address_space:  global
        .offset:         40
        .size:           8
        .value_kind:     global_buffer
      - .actual_access:  read_only
        .address_space:  global
        .offset:         48
        .size:           8
        .value_kind:     global_buffer
      - .actual_access:  read_only
        .address_space:  global
        .offset:         56
        .size:           8
        .value_kind:     global_buffer
      - .actual_access:  read_only
        .address_space:  global
        .offset:         64
        .size:           8
        .value_kind:     global_buffer
      - .actual_access:  write_only
        .address_space:  global
        .offset:         72
        .size:           8
        .value_kind:     global_buffer
    .group_segment_fixed_size: 0
    .kernarg_segment_align: 8
    .kernarg_segment_size: 80
    .language:       OpenCL C
    .language_version:
      - 2
      - 0
    .max_flat_workgroup_size: 256
    .name:           _Z8k_phase1PKfS0_S0_PDv4_jS2_PiS3_P15HIP_vector_typeIiLj2EES0_Pf
    .private_segment_fixed_size: 0
    .sgpr_count:     18
    .sgpr_spill_count: 0
    .symbol:         _Z8k_phase1PKfS0_S0_PDv4_jS2_PiS3_P15HIP_vector_typeIiLj2EES0_Pf.kd
    .uniform_work_group_size: 1
    .uses_dynamic_stack: false
    .vgpr_count:     19
    .vgpr_spill_count: 0
    .wavefront_size: 64
  - .agpr_count:     0
    .args:
      - .actual_access:  read_only
        .address_space:  global
        .offset:         0
        .size:           8
        .value_kind:     global_buffer
      - .actual_access:  read_only
        .address_space:  global
        .offset:         8
        .size:           8
        .value_kind:     global_buffer
      - .actual_access:  read_only
        .address_space:  global
        .offset:         16
        .size:           8
        .value_kind:     global_buffer
      - .actual_access:  read_only
        .address_space:  global
        .offset:         24
        .size:           8
        .value_kind:     global_buffer
      - .address_space:  global
        .offset:         32
        .size:           8
        .value_kind:     global_buffer
      - .actual_access:  write_only
        .address_space:  global
        .offset:         40
        .size:           8
        .value_kind:     global_buffer
      - .actual_access:  write_only
        .address_space:  global
        .offset:         48
        .size:           8
        .value_kind:     global_buffer
      - .actual_access:  write_only
        .address_space:  global
        .offset:         56
        .size:           8
        .value_kind:     global_buffer
      - .actual_access:  read_only
        .address_space:  global
        .offset:         64
        .size:           8
        .value_kind:     global_buffer
      - .actual_access:  write_only
        .address_space:  global
        .offset:         72
        .size:           8
        .value_kind:     global_buffer
      - .actual_access:  write_only
        .address_space:  global
        .offset:         80
        .size:           8
        .value_kind:     global_buffer
    .group_segment_fixed_size: 90112
    .kernarg_segment_align: 8
    .kernarg_segment_size: 88
    .language:       OpenCL C
    .language_version:
      - 2
      - 0
    .max_flat_workgroup_size: 768
    .name:           _Z7k_gemm1PKfS0_PKDv4_jPKiPiS6_P15HIP_vector_typeIiLj2EEPDF16_S0_S6_S9_
    .private_segment_fixed_size: 0
    .sgpr_count:     48
    .sgpr_spill_count: 0
    .symbol:         _Z7k_gemm1PKfS0_PKDv4_jPKiPiS6_P15HIP_vector_typeIiLj2EEPDF16_S0_S6_S9_.kd
    .uniform_work_group_size: 1
    .uses_dynamic_stack: false
    .vgpr_count:     168
    .vgpr_spill_count: 0
    .wavefront_size: 64
  - .agpr_count:     0
    .args:
      - .actual_access:  read_only
        .address_space:  global
        .offset:         0
        .size:           8
        .value_kind:     global_buffer
      - .actual_access:  read_only
        .address_space:  global
        .offset:         8
        .size:           8
        .value_kind:     global_buffer
      - .actual_access:  read_only
        .address_space:  global
        .offset:         16
        .size:           8
        .value_kind:     global_buffer
      - .actual_access:  read_only
        .address_space:  global
        .offset:         24
        .size:           8
        .value_kind:     global_buffer
      - .actual_access:  read_only
        .address_space:  global
        .offset:         32
        .size:           8
        .value_kind:     global_buffer
      - .actual_access:  read_only
        .address_space:  global
        .offset:         40
        .size:           8
        .value_kind:     global_buffer
      - .actual_access:  write_only
        .address_space:  global
        .offset:         48
        .size:           8
        .value_kind:     global_buffer
    .group_segment_fixed_size: 12576
    .kernarg_segment_align: 8
    .kernarg_segment_size: 56
    .language:       OpenCL C
    .language_version:
      - 2
      - 0
    .max_flat_workgroup_size: 256
    .name:           _Z8k_agg1g2PKDv4_jPKiS3_PK15HIP_vector_typeIiLj2EEPKfS1_PDF16_
    .private_segment_fixed_size: 0
    .sgpr_count:     52
    .sgpr_spill_count: 0
    .symbol:         _Z8k_agg1g2PKDv4_jPKiS3_PK15HIP_vector_typeIiLj2EEPKfS1_PDF16_.kd
    .uniform_work_group_size: 1
    .uses_dynamic_stack: false
    .vgpr_count:     126
    .vgpr_spill_count: 0
    .wavefront_size: 64
  - .agpr_count:     0
    .args:
      - .actual_access:  read_only
        .address_space:  global
        .offset:         0
        .size:           8
        .value_kind:     global_buffer
      - .actual_access:  read_only
        .address_space:  global
        .offset:         8
        .size:           8
        .value_kind:     global_buffer
      - .actual_access:  read_only
        .address_space:  global
        .offset:         16
        .size:           8
        .value_kind:     global_buffer
      - .actual_access:  read_only
        .address_space:  global
        .offset:         24
        .size:           8
        .value_kind:     global_buffer
      - .actual_access:  read_only
        .address_space:  global
        .offset:         32
        .size:           8
        .value_kind:     global_buffer
      - .actual_access:  write_only
        .address_space:  global
        .offset:         40
        .size:           8
        .value_kind:     global_buffer
      - .actual_access:  write_only
        .address_space:  global
        .offset:         48
        .size:           8
        .value_kind:     global_buffer
      - .actual_access:  write_only
        .address_space:  global
        .offset:         56
        .size:           8
        .value_kind:     global_buffer
    .group_segment_fixed_size: 0
    .kernarg_segment_align: 8
    .kernarg_segment_size: 64
    .language:       OpenCL C
    .language_version:
      - 2
      - 0
    .max_flat_workgroup_size: 256
    .name:           _Z6k_agg2PKDv4_jPKiS3_PK15HIP_vector_typeIiLj2EEPKfPfSA_PS_
    .private_segment_fixed_size: 0
    .sgpr_count:     18
    .sgpr_spill_count: 0
    .symbol:         _Z6k_agg2PKDv4_jPKiS3_PK15HIP_vector_typeIiLj2EEPKfPfSA_PS_.kd
    .uniform_work_group_size: 1
    .uses_dynamic_stack: false
    .vgpr_count:     74
    .vgpr_spill_count: 0
    .wavefront_size: 64
  - .agpr_count:     0
    .args:
      - .actual_access:  read_only
        .address_space:  global
        .offset:         0
        .size:           8
        .value_kind:     global_buffer
      - .actual_access:  read_only
        .address_space:  global
        .offset:         8
        .size:           8
        .value_kind:     global_buffer
      - .actual_access:  read_only
        .address_space:  global
        .offset:         16
        .size:           8
        .value_kind:     global_buffer
      - .actual_access:  read_only
        .address_space:  global
        .offset:         24
        .size:           8
        .value_kind:     global_buffer
      - .actual_access:  read_only
        .address_space:  global
        .offset:         32
        .size:           8
        .value_kind:     global_buffer
      - .actual_access:  read_only
        .address_space:  global
        .offset:         40
        .size:           8
        .value_kind:     global_buffer
      - .actual_access:  read_only
        .address_space:  global
        .offset:         48
        .size:           8
        .value_kind:     global_buffer
      - .actual_access:  write_only
        .address_space:  global
        .offset:         56
        .size:           8
        .value_kind:     global_buffer
      - .actual_access:  write_only
        .address_space:  global
        .offset:         64
        .size:           8
        .value_kind:     global_buffer
    .group_segment_fixed_size: 6144
    .kernarg_segment_align: 8
    .kernarg_segment_size: 72
    .language:       OpenCL C
    .language_version:
      - 2
      - 0
    .max_flat_workgroup_size: 256
    .name:           _Z9k_readoutPKDv4_jPKfPKiPK15HIP_vector_typeIiLj2EES3_S3_S3_PfSA_
    .private_segment_fixed_size: 0
    .sgpr_count:     20
    .sgpr_spill_count: 0
    .symbol:         _Z9k_readoutPKDv4_jPKfPKiPK15HIP_vector_typeIiLj2EES3_S3_S3_PfSA_.kd
    .uniform_work_group_size: 1
    .uses_dynamic_stack: false
    .vgpr_count:     92
    .vgpr_spill_count: 0
    .wavefront_size: 64
